# waves 0-2 of every workgroup convert one more gate_up sjob per attention step, staged through spare LDS by LDS-DMA (block jobs 4224..5759 moved out of phase 2)
# speedup vs baseline: 1.0039x; 1.0039x over previous
; #define LAS __attribute__((address_space(3)))
; __device__ __forceinline__ void conv_share_blk(const Args& a, LAS unsigned char* lds, int blk, int G) {
;     const int s = blk % 3, r = blk / 3, nb = (G - s + 2) / 3, nj = CONV_JOBS - BJOB0, j0 = BJOB0 + s * (nj / 3), j1 = (s == 2) ? CONV_JOBS : BJOB0 + (s + 1) * (nj / 3);
;     LAS unsigned char* Tlo = lds + 3 * 16384; LAS unsigned char* Thi = lds + LDS_EXTRA;
;     int j = j0 + r; if (j >= j1) return;
;     f32x4 v[16]; u32x4 o[4]; BJob cc = bjob_addr(a, j);
;     bjob_load(cc, v);
.LBB0_168:
	v_and_b32_e32 v1, 48, v0
	v_lshlrev_b32_e32 v2, 6, v0
	s_movk_i32 s2, 0x3c0
	s_add_u32 s14, s74, 0x3300000
	v_and_or_b32 v1, v2, s2, v1
	v_lshlrev_b32_e32 v2, 2, v0
	s_addc_u32 s15, s75, 0
	s_lshl_b32 s1, s5, 13
	v_and_b32_e32 v2, 32, v2
	v_bitop3_b32 v4, v1, s1, v2 bitop3:0xde
	s_lshl_b32 s1, s3, 5
	s_and_b32 s83, s1, 0x60
	s_lshl_b32 s82, s5, 6
	s_lshl_b32 s1, s83, 7
	s_sext_i32_i16 s6, s4
	s_add_u32 s4, s54, 0x80
	s_addc_u32 s5, s55, 0
	s_waitcnt vmcnt(4)
	s_barrier
	s_add_i32 m0, s78, 0x18000
	v_bitop3_b32 v1, s1, v1, v2 bitop3:0xf6
	v_lshl_add_u64 v[2:3], s[4:5], 0, v[130:131]
	s_add_u32 s4, s54, 0x40080
	s_addc_u32 s5, s55, 0
	global_load_lds_dwordx4 v[2:3], off
	s_add_i32 m0, s78, 0x1a000
	v_lshl_add_u64 v[2:3], s[4:5], 0, v[130:131]
	s_add_u32 s4, s56, 0x80
	s_addc_u32 s5, s57, 0
	global_load_lds_dwordx4 v[2:3], off
	s_add_i32 s84, s78, 0x8000
	v_lshl_add_u64 v[2:3], s[4:5], 0, v[132:133]
	s_add_u32 s4, s56, 0x40080
	s_mov_b32 m0, s84
	s_addc_u32 s5, s57, 0
	global_load_lds_dwordx4 v[2:3], off
	s_add_i32 s85, s78, 0xa000
	v_lshl_add_u64 v[2:3], s[4:5], 0, v[132:133]
	s_add_u32 s4, s54, 0x80080
	s_mov_b32 m0, s85
	s_addc_u32 s5, s55, 0
	global_load_lds_dwordx4 v[2:3], off
	s_add_i32 m0, s78, 0x1c000
	s_mul_hi_u32 s1, s96, 0xaaaaaaab
	v_lshl_add_u64 v[2:3], s[4:5], 0, v[130:131]
	s_add_u32 s4, s54, 0xc0080
	s_addc_u32 s5, s55, 0
	global_load_lds_dwordx4 v[2:3], off
	s_add_i32 m0, s78, 0x1e000
	v_lshl_add_u64 v[2:3], s[4:5], 0, v[130:131]
	global_load_lds_dwordx4 v[2:3], off
	s_lshr_b32 s1, s1, 1
	s_mul_i32 s1, s1, 3
	s_sub_i32 s86, s96, s1
	s_movk_i32 s1, 0x100
	v_cmp_gt_u32_e64 s[2:3], s1, v0
	s_mul_hi_i32 s1, s96, 0x55555556
	v_and_b32_e32 v2, 0x100, v0
	v_writelane_b32 v255, s2, 24
	v_cmp_ne_u32_e64 s[20:21], 0, v2
	s_waitcnt vmcnt(6)
	v_mov_b64_e32 v[136:137], 0x300
	v_writelane_b32 v255, s3, 25
	s_lshr_b32 s2, s1, 31
	s_add_i32 s1, s1, s2
	s_mul_i32 s2, s1, 3
	s_sub_i32 s2, s96, s2
	s_mul_i32 s3, s2, 0x330
	s_add_i32 s87, s3, 0x19b0
	s_min_i32 s87, s87, 0x2000
	s_add_i32 s3, s1, s3
	s_add_i32 s7, s3, 0x1680
	s_cmpk_lt_i32 s7, 0x2000
	s_cselect_b64 s[4:5], -1, 0
	s_waitcnt lgkmcnt(0)
	s_sub_i32 s2, s26, s2
	s_addk_i32 s3, 0xf080
	s_add_i32 s2, s2, 2
	s_lshr_b32 s12, s3, 7
	s_lshl_b32 s3, s7, 8
	s_lshl_b32 s8, s7, 4
	s_ashr_i32 s16, s7, 8
	s_lshl_b32 s7, s7, 3
	s_mul_hi_i32 s89, s2, 0x55555556
	s_and_b32 s22, s8, 0x780
	s_lshl_b64 s[8:9], s[12:13], 24
	s_lshl_b64 s[10:11], s[12:13], 22
	s_lshl_b32 s12, s1, 8
	s_ashr_i32 s17, s16, 31
	s_and_b32 s7, s7, 0x780
	s_lshr_b32 s2, s89, 31
	s_and_b32 s3, s3, 0x700
	s_lshl_b32 s23, s22, 13
	s_and_b32 s12, s12, 0xf00
	s_lshl_b64 s[18:19], s[16:17], 25
	s_lshl_b32 s24, s7, 14
	s_lshl_b64 s[16:17], s[16:17], 23
	v_writelane_b32 v255, s20, 26
	s_ashr_i32 s88, s26, 31
	s_add_i32 s89, s89, s2
	v_writelane_b32 v255, s21, 27
	s_and_b64 s[20:21], s[4:5], exec
	s_cselect_b32 s8, s18, s8
	s_cselect_b32 s90, s12, s3
	s_mov_b32 s3, 0xb300000
	s_cselect_b32 s10, s16, s10
	s_cselect_b32 s16, s46, s50
	s_cselect_b32 s2, s19, s9
	s_cselect_b32 s9, 0, 0
	s_cselect_b32 s18, s24, s23
	s_cselect_b32 s3, s3, 0x2b300000
	s_cselect_b32 s11, s17, s11
	s_cselect_b32 s7, s7, s22
	s_cselect_b32 s12, s47, s51
	s_add_u32 s8, s16, s8
	s_addc_u32 s2, s12, s2
	s_add_u32 s8, s8, s18
	s_addc_u32 s2, s2, s9
	s_lshl_b32 s12, s90, 2
	s_add_u32 s16, s8, s12
	s_addc_u32 s17, s2, 0
	s_add_u32 s2, s74, s3
	s_addc_u32 s3, s75, 0
	s_add_u32 s2, s2, s10
	s_addc_u32 s3, s3, s11
	s_add_u32 s18, s2, s7
	s_addc_u32 s19, s3, s9
	v_cndmask_b32_e64 v144, 0, 1, s[4:5]
	s_and_b64 s[4:5], s[4:5], exec
	s_cselect_b32 s91, 12, 11
	s_add_u32 s92, s74, 0x2b300000
	s_addc_u32 s93, s75, 0
	s_add_u32 s94, s74, 0xb300000
	s_mul_i32 s3, s96, 0x330
	s_mulk_i32 s1, 0x98f
	s_addc_u32 s95, s75, 0
	s_sub_i32 s2, s3, s1
	s_add_i32 s3, s89, s3
	s_sub_i32 s1, s3, s1
	s_add_i32 s1, s1, 0x1680
	v_writelane_b32 v255, s2, 28
	s_lshl_b32 s2, s1, 8
	s_add_i32 s29, 0, 0x10000
	s_add_i32 s24, 0, 0x14000
	v_writelane_b32 v255, s2, 29
	s_lshl_b32 s30, s89, 8
	s_lshl_b32 s31, s1, 4
	s_lshl_b32 s33, s89, 4
	s_lshl_b32 s3, s1, 3
	s_lshl_b32 s28, s89, 3
	v_mov_b64_e32 v[138:139], 0x2ff
	v_add_u32_e32 v145, s29, v1
	v_add_u32_e32 v146, 0, v4
	v_add_u32_e32 v147, s24, v1
	s_movk_i32 s25, 0x3000
	s_movk_i32 s77, 0x80
	s_mov_b32 s52, 0x3c800000
	s_add_i32 s53, 0, 0x20400
	s_movk_i32 s4, 0x7f
	s_mov_b32 s1, 0
	s_barrier
	s_branch .LBB0_171

; #define LAS __attribute__((address_space(3)))
; __device__ __forceinline__ void conv_share_blk(const Args& a, LAS unsigned char* lds, int blk, int G) {
;     const int s = blk % 3, r = blk / 3, nb = (G - s + 2) / 3, nj = CONV_JOBS - BJOB0, j0 = BJOB0 + s * (nj / 3), j1 = (s == 2) ? CONV_JOBS : BJOB0 + (s + 1) * (nj / 3);
;     LAS unsigned char* Tlo = lds + 3 * 16384; LAS unsigned char* Thi = lds + LDS_EXTRA;
;     int j = j0 + r; if (j >= j1) return;
;     f32x4 v[16]; u32x4 o[4]; BJob cc = bjob_addr(a, j);
;     bjob_load(cc, v);
; #pragma unroll 1
;     for (;;) {
;         bjob_pack(v, o);
;         const BJob cur = cc; const bool hn = (j + nb) < j1;
;         if (hn) { cc = bjob_addr(a, j + nb); bjob_load(cc, v); }
;         bjob_out(cur, o, Tlo, Thi);
;         if (!hn) break;
;         j += nb;
;     }
.LBB0_182:
	s_add_i32 s23, s89, s23
	s_add_i32 s62, s23, 0x1680
	s_cmp_ge_i32 s62, s87
	s_cselect_b64 s[56:57], -1, 0
	s_and_b64 vcc, exec, s[56:57]
	s_cbranch_vccnz .LBB0_181
	s_cmpk_gt_i32 s62, 0x1fff
	s_mov_b64 s[0:1], -1
	s_cbranch_scc0 .LBB0_185
	s_add_i32 s0, s23, 0xfffff080
	s_lshr_b32 s12, s0, 7
	s_and_b32 s54, s7, 0x780
	s_and_b32 s60, s21, 0x700
	s_lshl_b64 s[0:1], s[12:13], 24
	s_lshl_b32 s55, s54, 13
	s_add_u32 s0, s50, s0
	s_addc_u32 s1, s51, s1
	s_add_u32 s0, s0, s55
	s_addc_u32 s1, s1, 0
	s_lshl_b32 s55, s60, 2
	s_add_u32 s58, s0, s55
	s_addc_u32 s59, s1, 0
	s_lshl_b64 s[0:1], s[12:13], 22
	s_add_u32 s0, s92, s0
	s_addc_u32 s1, s93, s1
	s_add_u32 s54, s0, s54
	s_addc_u32 s55, s1, 0
	s_mov_b64 s[0:1], 0

; __device__ __forceinline__ unsigned pk4_fp8_scaled(float a, float b, float c, float d) { s16x2 r = {0, 0}; r = __builtin_amdgcn_cvt_scalef32_pk_fp8_f32(r, a, b, pg8::W8_INV, false); r = __builtin_amdgcn_cvt_scalef32_pk_fp8_f32(r, c, d, pg8::W8_INV, true); return __builtin_bit_cast(unsigned, r); }
; __device__ __forceinline__ SJob sjob_addr(const Args& a, int j, int lane) {
;     SJob c; const int kseg = lane & 7, nq = lane >> 3;
;     if (j < SJOBS_GU) { const int e = j >> 12, kb = (j >> 7) & 31, nb = j & 127, s0 = nb * 32, bj = s0 >> 11, rem = s0 & 2047, pn = rem >> 7, c0 = rem & 127, np = pn * 256 + bj * 128 + c0;
;         c.ld = 4096; c.src = a.w_gate_up + ((size_t)e * 2048 + kb * 64 + kseg * 8) * 4096 + s0 + nq * 4; c.dst = (unsigned char*)(a.ws + WS_WGU_T) + ((size_t)e * 4096 + np + nq * 4) * 2048 + kb * 64 + kseg * 8; }
;     else { const int jj = j - SJOBS_GU, e = jj >> 11, kb = (jj >> 6) & 31, nb = jj & 63;
;         c.ld = 2048; c.src = a.w_down + ((size_t)e * 2048 + kb * 64 + kseg * 8) * 2048 + nb * 32 + nq * 4; c.dst = (unsigned char*)(a.ws + WS_WD_T) + ((size_t)e * 2048 + nb * 32 + nq * 4) * 2048 + kb * 64 + kseg * 8; }
;     return c;
; }
; __device__ __forceinline__ void sjob_load(const SJob& c, f32x4 (&v)[8]) {
; #pragma unroll
;     for (int r = 0; r < 8; ++r) v[r] = __builtin_nontemporal_load((const f32x4*)(c.src + (size_t)r * c.ld));
; }
; __device__ __forceinline__ void sjob_store(const SJob& c, const f32x4 (&v)[8]) {
; #pragma unroll
;     for (int jn = 0; jn < 4; ++jn) { u32x2 o;
;         o.x = pk4_fp8_scaled(v[0][jn], v[1][jn], v[2][jn], v[3][jn]); o.y = pk4_fp8_scaled(v[4][jn], v[5][jn], v[6][jn], v[7][jn]);
;         __builtin_nontemporal_store(o, (u32x2*)(c.dst + (size_t)jn * 2048)); }
; }
.LBB0_436:
	s_or_b64 exec, exec, s[16:17]
	v_readfirstlane_b32 s85, v167
	s_nop 3
	s_cmp_lt_u32 s85, 3
	s_cbranch_scc0 .Lxa_ne
	s_cmp_eq_u32 s84, -1
	s_cbranch_scc1 .Lxa_ne
	s_waitcnt vmcnt(0)
	s_lshr_b32 s8, s84, 12
	s_bfe_u32 s9, s84, 0x50007
	s_and_b32 s10, s84, 0x7f
	s_bfe_u32 s11, s10, 0x40002
	s_lshl_b32 s11, s11, 8
	s_lshr_b32 s16, s10, 6
	s_lshl_b32 s16, s16, 7
	s_add_i32 s11, s11, s16
	s_and_b32 s16, s10, 3
	s_lshl_b32 s16, s16, 5
	s_add_i32 s11, s11, s16
	s_lshl_b32 s16, s8, 23
	s_lshl_b32 s11, s11, 11
	s_add_u32 s16, s16, s11
	s_lshl_b32 s11, s9, 6
	s_add_u32 s16, s16, s11
	s_add_u32 s16, s16, 0xb300000
	s_add_u32 s16, s74, s16
	s_addc_u32 s17, s75, 0
	v_lshlrev_b32_e32 v131, 11, v180
	v_add_u32_e32 v131, v131, v178
	v_and_b32_e32 v130, 63, v0
	v_lshlrev_b32_e32 v130, 4, v130
	s_lshl_b32 s86, s85, 13
	s_add_i32 s86, s86, 0x20400
	v_add_u32_e32 v130, s86, v130
	ds_read_b32 v132, v130 offset:0
	ds_read_b32 v133, v130 offset:1024
	ds_read_b32 v134, v130 offset:2048
	ds_read_b32 v135, v130 offset:3072
	s_waitcnt lgkmcnt(0)
	v_cvt_scalef32_pk_fp8_f32 v136, v132, v133, s23
	v_cvt_scalef32_pk_fp8_f32 v136, v134, v135, s23 op_sel:[0,0,0,1]
	ds_read_b32 v132, v130 offset:4096
	ds_read_b32 v133, v130 offset:5120
	ds_read_b32 v134, v130 offset:6144
	ds_read_b32 v135, v130 offset:7168
	s_waitcnt lgkmcnt(0)
	v_cvt_scalef32_pk_fp8_f32 v137, v132, v133, s23
	v_cvt_scalef32_pk_fp8_f32 v137, v134, v135, s23 op_sel:[0,0,0,1]
	global_store_dwordx2 v131, v[136:137], s[16:17] nt
	ds_read_b32 v132, v130 offset:4
	ds_read_b32 v133, v130 offset:1028
	ds_read_b32 v134, v130 offset:2052
	ds_read_b32 v135, v130 offset:3076
	s_waitcnt lgkmcnt(0)
	v_cvt_scalef32_pk_fp8_f32 v136, v132, v133, s23
	v_cvt_scalef32_pk_fp8_f32 v136, v134, v135, s23 op_sel:[0,0,0,1]
	ds_read_b32 v132, v130 offset:4100
	ds_read_b32 v133, v130 offset:5124
	ds_read_b32 v134, v130 offset:6148
	ds_read_b32 v135, v130 offset:7172
	s_waitcnt lgkmcnt(0)
	v_cvt_scalef32_pk_fp8_f32 v137, v132, v133, s23
	v_cvt_scalef32_pk_fp8_f32 v137, v134, v135, s23 op_sel:[0,0,0,1]
	global_store_dwordx2 v131, v[136:137], s[16:17] offset:2048 nt
	ds_read_b32 v132, v130 offset:8
	ds_read_b32 v133, v130 offset:1032
	ds_read_b32 v134, v130 offset:2056
	ds_read_b32 v135, v130 offset:3080
	s_waitcnt lgkmcnt(0)
	v_cvt_scalef32_pk_fp8_f32 v136, v132, v133, s23
	v_cvt_scalef32_pk_fp8_f32 v136, v134, v135, s23 op_sel:[0,0,0,1]
	ds_read_b32 v132, v130 offset:4104
	ds_read_b32 v133, v130 offset:5128
	ds_read_b32 v134, v130 offset:6152
	ds_read_b32 v135, v130 offset:7176
	s_waitcnt lgkmcnt(0)
	v_cvt_scalef32_pk_fp8_f32 v137, v132, v133, s23
	v_cvt_scalef32_pk_fp8_f32 v137, v134, v135, s23 op_sel:[0,0,0,1]
	s_add_u32 s16, s16, 0x1000
	s_addc_u32 s17, s17, 0
	global_store_dwordx2 v131, v[136:137], s[16:17] nt
	ds_read_b32 v132, v130 offset:12
	ds_read_b32 v133, v130 offset:1036
	ds_read_b32 v134, v130 offset:2060
	ds_read_b32 v135, v130 offset:3084
	s_waitcnt lgkmcnt(0)
	v_cvt_scalef32_pk_fp8_f32 v136, v132, v133, s23
	v_cvt_scalef32_pk_fp8_f32 v136, v134, v135, s23 op_sel:[0,0,0,1]
	ds_read_b32 v132, v130 offset:4108
	ds_read_b32 v133, v130 offset:5132
	ds_read_b32 v134, v130 offset:6156
	ds_read_b32 v135, v130 offset:7180
	s_waitcnt lgkmcnt(0)
	v_cvt_scalef32_pk_fp8_f32 v137, v132, v133, s23
	v_cvt_scalef32_pk_fp8_f32 v137, v134, v135, s23 op_sel:[0,0,0,1]
	global_store_dwordx2 v131, v[136:137], s[16:17] offset:2048 nt

; __device__ __forceinline__ SJob sjob_addr(const Args& a, int j, int lane) {
;     SJob c; const int kseg = lane & 7, nq = lane >> 3;
;     if (j < SJOBS_GU) { const int e = j >> 12, kb = (j >> 7) & 31, nb = j & 127, s0 = nb * 32, bj = s0 >> 11, rem = s0 & 2047, pn = rem >> 7, c0 = rem & 127, np = pn * 256 + bj * 128 + c0;
;         c.ld = 4096; c.src = a.w_gate_up + ((size_t)e * 2048 + kb * 64 + kseg * 8) * 4096 + s0 + nq * 4; c.dst = (unsigned char*)(a.ws + WS_WGU_T) + ((size_t)e * 4096 + np + nq * 4) * 2048 + kb * 64 + kseg * 8; }
;     else { const int jj = j - SJOBS_GU, e = jj >> 11, kb = (jj >> 6) & 31, nb = jj & 63;
;         c.ld = 2048; c.src = a.w_down + ((size_t)e * 2048 + kb * 64 + kseg * 8) * 2048 + nb * 32 + nq * 4; c.dst = (unsigned char*)(a.ws + WS_WD_T) + ((size_t)e * 2048 + nb * 32 + nq * 4) * 2048 + kb * 64 + kseg * 8; }
;     return c;
; }
; __device__ __forceinline__ void sjob_load(const SJob& c, f32x4 (&v)[8]) {
; #pragma unroll
;     for (int r = 0; r < 8; ++r) v[r] = __builtin_nontemporal_load((const f32x4*)(c.src + (size_t)r * c.ld));
; }
.LBB0_447:
	v_readfirstlane_b32 s85, v167
	s_nop 3
	s_cmp_lt_u32 s85, 3
	s_cbranch_scc0 .Lxa_ni
	s_add_i32 s84, s59, -1
	s_cmp_lt_u32 s84, 32
	s_cbranch_scc1 .Lxa_go
	s_mov_b32 s84, -1
	s_branch .Lxa_ni
.Lxa_go:
	s_mul_i32 s84, s84, 0x300
	s_mul_i32 s86, s38, 3
	s_add_i32 s84, s84, s86
	s_add_i32 s84, s84, s85
	s_add_i32 s84, s84, 0x10800
	s_lshr_b32 s86, s84, 12
	s_bfe_u32 s87, s84, 0x50007
	s_and_b32 s88, s84, 0x7f
	s_lshl_b32 s86, s86, 25
	s_lshl_b32 s87, s87, 20
	s_add_u32 s86, s86, s87
	s_lshl_b32 s88, s88, 7
	s_add_u32 s86, s86, s88
	s_add_u32 s86, s46, s86
	s_addc_u32 s87, s47, 0
	v_lshlrev_b32_e32 v135, 14, v178
	v_add_u32_e32 v135, v135, v168
	s_lshl_b32 s88, s85, 13
	s_add_i32 s88, s88, 0x20400
	s_mov_b32 m0, s88
	s_nop 0
	global_load_lds_dwordx4 v135, s[86:87] nt
	s_add_u32 s86, s86, 0x4000
	s_addc_u32 s87, s87, 0
	s_add_i32 s88, s88, 0x400
	s_mov_b32 m0, s88
	s_nop 0
	global_load_lds_dwordx4 v135, s[86:87] nt
	s_add_u32 s86, s86, 0x4000
	s_addc_u32 s87, s87, 0
	s_add_i32 s88, s88, 0x400
	s_mov_b32 m0, s88
	s_nop 0
	global_load_lds_dwordx4 v135, s[86:87] nt
	s_add_u32 s86, s86, 0x4000
	s_addc_u32 s87, s87, 0
	s_add_i32 s88, s88, 0x400
	s_mov_b32 m0, s88
	s_nop 0
	global_load_lds_dwordx4 v135, s[86:87] nt
	s_add_u32 s86, s86, 0x4000
	s_addc_u32 s87, s87, 0
	s_add_i32 s88, s88, 0x400
	s_mov_b32 m0, s88
	s_nop 0
	global_load_lds_dwordx4 v135, s[86:87] nt
	s_add_u32 s86, s86, 0x4000
	s_addc_u32 s87, s87, 0
	s_add_i32 s88, s88, 0x400
	s_mov_b32 m0, s88
	s_nop 0
	global_load_lds_dwordx4 v135, s[86:87] nt
	s_add_u32 s86, s86, 0x4000
	s_addc_u32 s87, s87, 0
	s_add_i32 s88, s88, 0x400
	s_mov_b32 m0, s88
	s_nop 0
	global_load_lds_dwordx4 v135, s[86:87] nt
	s_add_u32 s86, s86, 0x4000
	s_addc_u32 s87, s87, 0
	s_add_i32 s88, s88, 0x400
	s_mov_b32 m0, s88
	s_nop 0
	global_load_lds_dwordx4 v135, s[86:87] nt

; __device__ __forceinline__ unsigned pk4_fp8_scaled(float a, float b, float c, float d) { s16x2 r = {0, 0}; r = __builtin_amdgcn_cvt_scalef32_pk_fp8_f32(r, a, b, pg8::W8_INV, false); r = __builtin_amdgcn_cvt_scalef32_pk_fp8_f32(r, c, d, pg8::W8_INV, true); return __builtin_bit_cast(unsigned, r); }
; __device__ __forceinline__ SJob sjob_addr(const Args& a, int j, int lane) {
;     SJob c; const int kseg = lane & 7, nq = lane >> 3;
;     if (j < SJOBS_GU) { const int e = j >> 12, kb = (j >> 7) & 31, nb = j & 127, s0 = nb * 32, bj = s0 >> 11, rem = s0 & 2047, pn = rem >> 7, c0 = rem & 127, np = pn * 256 + bj * 128 + c0;
;         c.ld = 4096; c.src = a.w_gate_up + ((size_t)e * 2048 + kb * 64 + kseg * 8) * 4096 + s0 + nq * 4; c.dst = (unsigned char*)(a.ws + WS_WGU_T) + ((size_t)e * 4096 + np + nq * 4) * 2048 + kb * 64 + kseg * 8; }
;     else { const int jj = j - SJOBS_GU, e = jj >> 11, kb = (jj >> 6) & 31, nb = jj & 63;
;         c.ld = 2048; c.src = a.w_down + ((size_t)e * 2048 + kb * 64 + kseg * 8) * 2048 + nb * 32 + nq * 4; c.dst = (unsigned char*)(a.ws + WS_WD_T) + ((size_t)e * 2048 + nb * 32 + nq * 4) * 2048 + kb * 64 + kseg * 8; }
;     return c;
; }
; __device__ __forceinline__ void sjob_load(const SJob& c, f32x4 (&v)[8]) {
; #pragma unroll
;     for (int r = 0; r < 8; ++r) v[r] = __builtin_nontemporal_load((const f32x4*)(c.src + (size_t)r * c.ld));
; }
; __device__ __forceinline__ void sjob_store(const SJob& c, const f32x4 (&v)[8]) {
; #pragma unroll
;     for (int jn = 0; jn < 4; ++jn) { u32x2 o;
;         o.x = pk4_fp8_scaled(v[0][jn], v[1][jn], v[2][jn], v[3][jn]); o.y = pk4_fp8_scaled(v[4][jn], v[5][jn], v[6][jn], v[7][jn]);
;         __builtin_nontemporal_store(o, (u32x2*)(c.dst + (size_t)jn * 2048)); }
; }
.LBB0_473:
	s_or_b64 exec, exec, s[16:17]
	v_readfirstlane_b32 s85, v167
	s_nop 3
	s_cmp_lt_u32 s85, 3
	s_cbranch_scc0 .Lxb_ne
	s_cmp_eq_u32 s84, -1
	s_cbranch_scc1 .Lxb_ne
	s_waitcnt vmcnt(0)
	s_lshr_b32 s8, s84, 12
	s_bfe_u32 s9, s84, 0x50007
	s_and_b32 s10, s84, 0x7f
	s_bfe_u32 s11, s10, 0x40002
	s_lshl_b32 s11, s11, 8
	s_lshr_b32 s16, s10, 6
	s_lshl_b32 s16, s16, 7
	s_add_i32 s11, s11, s16
	s_and_b32 s16, s10, 3
	s_lshl_b32 s16, s16, 5
	s_add_i32 s11, s11, s16
	s_lshl_b32 s16, s8, 23
	s_lshl_b32 s11, s11, 11
	s_add_u32 s16, s16, s11
	s_lshl_b32 s11, s9, 6
	s_add_u32 s16, s16, s11
	s_add_u32 s16, s16, 0xb300000
	s_add_u32 s16, s74, s16
	s_addc_u32 s17, s75, 0
	v_lshlrev_b32_e32 v37, 11, v180
	v_add_u32_e32 v37, v37, v178
	v_and_b32_e32 v36, 63, v0
	v_lshlrev_b32_e32 v36, 4, v36
	s_lshl_b32 s86, s85, 13
	s_add_i32 s86, s86, 0x20400
	v_add_u32_e32 v36, s86, v36
	ds_read_b32 v134, v36 offset:0
	ds_read_b32 v135, v36 offset:1024
	ds_read_b32 v136, v36 offset:2048
	ds_read_b32 v137, v36 offset:3072
	s_waitcnt lgkmcnt(0)
	v_cvt_scalef32_pk_fp8_f32 v138, v134, v135, s23
	v_cvt_scalef32_pk_fp8_f32 v138, v136, v137, s23 op_sel:[0,0,0,1]
	ds_read_b32 v134, v36 offset:4096
	ds_read_b32 v135, v36 offset:5120
	ds_read_b32 v136, v36 offset:6144
	ds_read_b32 v137, v36 offset:7168
	s_waitcnt lgkmcnt(0)
	v_cvt_scalef32_pk_fp8_f32 v139, v134, v135, s23
	v_cvt_scalef32_pk_fp8_f32 v139, v136, v137, s23 op_sel:[0,0,0,1]
	global_store_dwordx2 v37, v[138:139], s[16:17] nt
	ds_read_b32 v134, v36 offset:4
	ds_read_b32 v135, v36 offset:1028
	ds_read_b32 v136, v36 offset:2052
	ds_read_b32 v137, v36 offset:3076
	s_waitcnt lgkmcnt(0)
	v_cvt_scalef32_pk_fp8_f32 v138, v134, v135, s23
	v_cvt_scalef32_pk_fp8_f32 v138, v136, v137, s23 op_sel:[0,0,0,1]
	ds_read_b32 v134, v36 offset:4100
	ds_read_b32 v135, v36 offset:5124
	ds_read_b32 v136, v36 offset:6148
	ds_read_b32 v137, v36 offset:7172
	s_waitcnt lgkmcnt(0)
	v_cvt_scalef32_pk_fp8_f32 v139, v134, v135, s23
	v_cvt_scalef32_pk_fp8_f32 v139, v136, v137, s23 op_sel:[0,0,0,1]
	global_store_dwordx2 v37, v[138:139], s[16:17] offset:2048 nt
	ds_read_b32 v134, v36 offset:8
	ds_read_b32 v135, v36 offset:1032
	ds_read_b32 v136, v36 offset:2056
	ds_read_b32 v137, v36 offset:3080
	s_waitcnt lgkmcnt(0)
	v_cvt_scalef32_pk_fp8_f32 v138, v134, v135, s23
	v_cvt_scalef32_pk_fp8_f32 v138, v136, v137, s23 op_sel:[0,0,0,1]
	ds_read_b32 v134, v36 offset:4104
	ds_read_b32 v135, v36 offset:5128
	ds_read_b32 v136, v36 offset:6152
	ds_read_b32 v137, v36 offset:7176
	s_waitcnt lgkmcnt(0)
	v_cvt_scalef32_pk_fp8_f32 v139, v134, v135, s23
	v_cvt_scalef32_pk_fp8_f32 v139, v136, v137, s23 op_sel:[0,0,0,1]
	s_add_u32 s16, s16, 0x1000
	s_addc_u32 s17, s17, 0
	global_store_dwordx2 v37, v[138:139], s[16:17] nt
	ds_read_b32 v134, v36 offset:12
	ds_read_b32 v135, v36 offset:1036
	ds_read_b32 v136, v36 offset:2060
	ds_read_b32 v137, v36 offset:3084
	s_waitcnt lgkmcnt(0)
	v_cvt_scalef32_pk_fp8_f32 v138, v134, v135, s23
	v_cvt_scalef32_pk_fp8_f32 v138, v136, v137, s23 op_sel:[0,0,0,1]
	ds_read_b32 v134, v36 offset:4108
	ds_read_b32 v135, v36 offset:5132
	ds_read_b32 v136, v36 offset:6156
	ds_read_b32 v137, v36 offset:7180
	s_waitcnt lgkmcnt(0)
	v_cvt_scalef32_pk_fp8_f32 v139, v134, v135, s23
	v_cvt_scalef32_pk_fp8_f32 v139, v136, v137, s23 op_sel:[0,0,0,1]
	global_store_dwordx2 v37, v[138:139], s[16:17] offset:2048 nt

; __device__ __forceinline__ SJob sjob_addr(const Args& a, int j, int lane) {
;     SJob c; const int kseg = lane & 7, nq = lane >> 3;
;     if (j < SJOBS_GU) { const int e = j >> 12, kb = (j >> 7) & 31, nb = j & 127, s0 = nb * 32, bj = s0 >> 11, rem = s0 & 2047, pn = rem >> 7, c0 = rem & 127, np = pn * 256 + bj * 128 + c0;
;         c.ld = 4096; c.src = a.w_gate_up + ((size_t)e * 2048 + kb * 64 + kseg * 8) * 4096 + s0 + nq * 4; c.dst = (unsigned char*)(a.ws + WS_WGU_T) + ((size_t)e * 4096 + np + nq * 4) * 2048 + kb * 64 + kseg * 8; }
;     else { const int jj = j - SJOBS_GU, e = jj >> 11, kb = (jj >> 6) & 31, nb = jj & 63;
;         c.ld = 2048; c.src = a.w_down + ((size_t)e * 2048 + kb * 64 + kseg * 8) * 2048 + nb * 32 + nq * 4; c.dst = (unsigned char*)(a.ws + WS_WD_T) + ((size_t)e * 2048 + nb * 32 + nq * 4) * 2048 + kb * 64 + kseg * 8; }
;     return c;
; }
; __device__ __forceinline__ void sjob_load(const SJob& c, f32x4 (&v)[8]) {
; #pragma unroll
;     for (int r = 0; r < 8; ++r) v[r] = __builtin_nontemporal_load((const f32x4*)(c.src + (size_t)r * c.ld));
; }
.LBB0_484:
	v_readfirstlane_b32 s85, v167
	s_nop 3
	s_cmp_lt_u32 s85, 3
	s_cbranch_scc0 .Lxb_ni
	s_lshr_b32 s86, s38, 4
	s_sub_i32 s84, 31, s86
	s_add_i32 s84, s84, s58
	s_cmp_lt_u32 s84, 32
	s_cbranch_scc1 .Lxb_go
	s_mov_b32 s84, -1
	s_branch .Lxb_ni
.Lxb_go:
	s_mul_i32 s84, s84, 0x300
	s_mul_i32 s86, s38, 3
	s_add_i32 s84, s84, s86
	s_add_i32 s84, s84, s85
	s_add_i32 s84, s84, 0x10800
	s_lshr_b32 s86, s84, 12
	s_bfe_u32 s87, s84, 0x50007
	s_and_b32 s88, s84, 0x7f
	s_lshl_b32 s86, s86, 25
	s_lshl_b32 s87, s87, 20
	s_add_u32 s86, s86, s87
	s_lshl_b32 s88, s88, 7
	s_add_u32 s86, s86, s88
	s_add_u32 s86, s46, s86
	s_addc_u32 s87, s47, 0
	v_lshlrev_b32_e32 v139, 14, v178
	v_add_u32_e32 v139, v139, v168
	s_lshl_b32 s88, s85, 13
	s_add_i32 s88, s88, 0x20400
	s_mov_b32 m0, s88
	s_nop 0
	global_load_lds_dwordx4 v139, s[86:87] nt
	s_add_u32 s86, s86, 0x4000
	s_addc_u32 s87, s87, 0
	s_add_i32 s88, s88, 0x400
	s_mov_b32 m0, s88
	s_nop 0
	global_load_lds_dwordx4 v139, s[86:87] nt
	s_add_u32 s86, s86, 0x4000
	s_addc_u32 s87, s87, 0
	s_add_i32 s88, s88, 0x400
	s_mov_b32 m0, s88
	s_nop 0
	global_load_lds_dwordx4 v139, s[86:87] nt
	s_add_u32 s86, s86, 0x4000
	s_addc_u32 s87, s87, 0
	s_add_i32 s88, s88, 0x400
	s_mov_b32 m0, s88
	s_nop 0
	global_load_lds_dwordx4 v139, s[86:87] nt
	s_add_u32 s86, s86, 0x4000
	s_addc_u32 s87, s87, 0
	s_add_i32 s88, s88, 0x400
	s_mov_b32 m0, s88
	s_nop 0
	global_load_lds_dwordx4 v139, s[86:87] nt
	s_add_u32 s86, s86, 0x4000
	s_addc_u32 s87, s87, 0
	s_add_i32 s88, s88, 0x400
	s_mov_b32 m0, s88
	s_nop 0
	global_load_lds_dwordx4 v139, s[86:87] nt
	s_add_u32 s86, s86, 0x4000
	s_addc_u32 s87, s87, 0
	s_add_i32 s88, s88, 0x400
	s_mov_b32 m0, s88
	s_nop 0
	global_load_lds_dwordx4 v139, s[86:87] nt
	s_add_u32 s86, s86, 0x4000
	s_addc_u32 s87, s87, 0
	s_add_i32 s88, s88, 0x400
	s_mov_b32 m0, s88
	s_nop 0
	global_load_lds_dwordx4 v139, s[86:87] nt
